# accumulator zeroing moved from the serial unit-boundary code into the first K iteration's load segments (P1, P7, P8 loops)
# baseline (speedup 1.0000x reference)
.LBB0_197:
	s_and_b64 s[6:7], s[30:31], exec
	s_cselect_b32 s5, s25, s35
	s_cselect_b32 s11, s24, s34
	s_cselect_b32 s21, s27, s63
	s_cselect_b32 s23, s26, s62
	s_cselect_b32 vcc_lo, s29, s37
	s_cselect_b32 vcc_hi, s28, s36
	s_add_u32 s8, s62, 0x100
	s_addc_u32 s6, s63, 0
	s_add_u32 s7, s36, 0x100
	s_addc_u32 s33, s37, 0
	s_mov_b32 s9, -2
.LBB0_198:
	ds_read_b128 v[146:149], v140
	ds_read_b128 v[150:153], v140 offset:1024
	ds_read_b128 v[154:157], v140 offset:2048
	ds_read_b128 v[158:161], v140 offset:3072
	ds_read_b128 v[162:165], v141
	ds_read_b128 v[166:169], v141 offset:1024
	ds_read_b128 v[170:173], v141 offset:2048
	ds_read_b128 v[174:177], v141 offset:3072
	s_add_u32 s36, s34, 0x100
	s_addc_u32 s37, s35, 0
	s_cmp_eq_u32 s9, 12
	s_cselect_b32 s84, s23, s8
	s_cselect_b32 s85, s21, s6
	s_cselect_b32 s63, vcc_lo, s33
	s_cselect_b32 s62, vcc_hi, s7
	s_cselect_b32 s80, s11, s36
	s_cselect_b32 s81, s5, s37
	s_add_u32 s78, s84, 0x80
	s_addc_u32 s79, s85, 0
	s_add_u32 s76, s80, 0x80
	s_addc_u32 s77, s81, 0
	ds_read_b128 v[178:181], v142
	ds_read_b128 v[182:185], v142 offset:1024
	ds_read_b128 v[186:189], v142 offset:2048
	ds_read_b128 v[190:193], v142 offset:3072
	ds_read_b128 v[194:197], v142 offset:4096
	ds_read_b128 v[198:201], v142 offset:5120
	ds_read_b128 v[202:205], v142 offset:6144
	ds_read_b128 v[206:209], v142 offset:7168
	s_add_u32 s34, s34, 0x40080
	s_addc_u32 s35, s35, 0
	s_mov_b32 s0, m0
	s_mov_b32 m0, s53
	s_nop 2
	global_load_lds_dwordx4 v138, s[34:35]
	s_mov_b32 m0, s0
	s_nop 0
	s_mov_b32 s0, m0
	s_mov_b32 m0, s54
	s_nop 2
	global_load_lds_dwordx4 v139, s[34:35]
	s_mov_b32 m0, s0
	s_cmp_lg_u32 s9, -2
	s_cbranch_scc1 .Lz1_a
	v_mov_b32_e32 v124, 0
	v_mov_b32_e32 v125, 0
	v_pk_mov_b32 v[126:127], v[124:125], v[124:125]
	v_pk_mov_b32 v[120:121], v[124:125], v[124:125]
	v_pk_mov_b32 v[122:123], v[124:125], v[124:125]
	v_pk_mov_b32 v[108:109], v[124:125], v[124:125]
	v_pk_mov_b32 v[110:111], v[124:125], v[124:125]
	v_pk_mov_b32 v[104:105], v[124:125], v[124:125]
	v_pk_mov_b32 v[106:107], v[124:125], v[124:125]
	v_pk_mov_b32 v[92:93], v[124:125], v[124:125]
	v_pk_mov_b32 v[94:95], v[124:125], v[124:125]
	v_pk_mov_b32 v[88:89], v[124:125], v[124:125]
	v_pk_mov_b32 v[90:91], v[124:125], v[124:125]
	v_pk_mov_b32 v[76:77], v[124:125], v[124:125]
	v_pk_mov_b32 v[78:79], v[124:125], v[124:125]
	v_pk_mov_b32 v[72:73], v[124:125], v[124:125]
	v_pk_mov_b32 v[74:75], v[124:125], v[124:125]
	v_pk_mov_b32 v[116:117], v[124:125], v[124:125]
	v_pk_mov_b32 v[118:119], v[124:125], v[124:125]
	v_pk_mov_b32 v[112:113], v[124:125], v[124:125]
	v_pk_mov_b32 v[114:115], v[124:125], v[124:125]
	v_pk_mov_b32 v[100:101], v[124:125], v[124:125]
	v_pk_mov_b32 v[102:103], v[124:125], v[124:125]
	v_pk_mov_b32 v[96:97], v[124:125], v[124:125]
	v_pk_mov_b32 v[98:99], v[124:125], v[124:125]
	v_pk_mov_b32 v[84:85], v[124:125], v[124:125]
	v_pk_mov_b32 v[86:87], v[124:125], v[124:125]
	v_pk_mov_b32 v[80:81], v[124:125], v[124:125]
	v_pk_mov_b32 v[82:83], v[124:125], v[124:125]
	v_pk_mov_b32 v[68:69], v[124:125], v[124:125]
	v_pk_mov_b32 v[70:71], v[124:125], v[124:125]
	v_pk_mov_b32 v[64:65], v[124:125], v[124:125]
	v_pk_mov_b32 v[66:67], v[124:125], v[124:125]
.Lz1_a:
	s_waitcnt vmcnt(8)
	s_waitcnt lgkmcnt(0)
	s_barrier
	s_setprio 1
	s_waitcnt lgkmcnt(6)
	v_mfma_scale_f32_16x16x128_f8f6f4 v[124:127], v[146:153], v[178:185], v[124:127], v143, v143 op_sel_hi:[0,0,0]
	v_mfma_scale_f32_16x16x128_f8f6f4 v[120:123], v[154:161], v[178:185], v[120:123], v143, v143 op_sel_hi:[0,0,0]
	s_waitcnt lgkmcnt(4)
	v_mfma_scale_f32_16x16x128_f8f6f4 v[108:111], v[146:153], v[186:193], v[108:111], v143, v143 op_sel_hi:[0,0,0]
	v_mfma_scale_f32_16x16x128_f8f6f4 v[104:107], v[154:161], v[186:193], v[104:107], v143, v143 op_sel_hi:[0,0,0]
	s_waitcnt lgkmcnt(2)
	v_mfma_scale_f32_16x16x128_f8f6f4 v[130:133], v[146:153], v[194:201], v[92:95], v143, v143 op_sel_hi:[0,0,0]
	v_mfma_scale_f32_16x16x128_f8f6f4 v[210:213], v[154:161], v[194:201], v[88:91], v143, v143 op_sel_hi:[0,0,0]
	s_waitcnt lgkmcnt(0)
	v_mfma_scale_f32_16x16x128_f8f6f4 v[214:217], v[146:153], v[202:209], v[76:79], v143, v143 op_sel_hi:[0,0,0]
	v_mfma_scale_f32_16x16x128_f8f6f4 v[218:221], v[154:161], v[202:209], v[72:75], v143, v143 op_sel_hi:[0,0,0]
	s_setprio 0
	s_setprio 1
	v_mfma_scale_f32_16x16x128_f8f6f4 v[116:119], v[162:169], v[178:185], v[116:119], v143, v143 op_sel_hi:[0,0,0]
	v_mfma_scale_f32_16x16x128_f8f6f4 v[112:115], v[170:177], v[178:185], v[112:115], v143, v143 op_sel_hi:[0,0,0]
	v_mfma_scale_f32_16x16x128_f8f6f4 v[100:103], v[162:169], v[186:193], v[100:103], v143, v143 op_sel_hi:[0,0,0]
	v_mfma_scale_f32_16x16x128_f8f6f4 v[96:99], v[170:177], v[186:193], v[96:99], v143, v143 op_sel_hi:[0,0,0]
	v_mfma_scale_f32_16x16x128_f8f6f4 v[178:181], v[162:169], v[194:201], v[84:87], v143, v143 op_sel_hi:[0,0,0]
	v_mfma_scale_f32_16x16x128_f8f6f4 v[182:185], v[170:177], v[194:201], v[80:83], v143, v143 op_sel_hi:[0,0,0]
	v_mfma_scale_f32_16x16x128_f8f6f4 v[186:189], v[162:169], v[202:209], v[68:71], v143, v143 op_sel_hi:[0,0,0]
	v_mfma_scale_f32_16x16x128_f8f6f4 v[190:193], v[170:177], v[202:209], v[64:67], v143, v143 op_sel_hi:[0,0,0]
	s_setprio 0
	s_barrier
	s_nop 4
	ds_read_b128 v[64:67], v142 offset:16384
	ds_read_b128 v[68:71], v142 offset:17408
	ds_read_b128 v[72:75], v142 offset:18432
	ds_read_b128 v[76:79], v142 offset:19456
	ds_read_b128 v[80:83], v142 offset:20480
	ds_read_b128 v[84:87], v142 offset:21504
	ds_read_b128 v[88:91], v142 offset:22528
	ds_read_b128 v[92:95], v142 offset:23552
	s_mov_b32 s0, m0
	s_mov_b32 m0, s19
	s_nop 2
	global_load_lds_dwordx4 v136, s[84:85]
	s_mov_b32 m0, s0
	s_nop 0
	s_mov_b32 s0, m0
	s_mov_b32 m0, s40
	s_nop 2
	global_load_lds_dwordx4 v137, s[84:85]
	s_mov_b32 m0, s0
	s_nop 0
	s_mov_b32 s0, m0
	s_mov_b32 m0, s41
	s_nop 2
	global_load_lds_dwordx4 v136, s[62:63]
	s_mov_b32 m0, s0
	s_nop 0
	s_mov_b32 s0, m0
	s_mov_b32 m0, s42
	s_nop 2
	global_load_lds_dwordx4 v137, s[62:63]
	s_mov_b32 m0, s0
	s_nop 0
	s_mov_b32 s0, m0
	s_mov_b32 m0, s97
	s_nop 2
	global_load_lds_dwordx4 v138, s[80:81]
	s_mov_b32 m0, s0
	s_nop 0
	s_mov_b32 s0, m0
	s_mov_b32 m0, s43
	s_nop 2
	global_load_lds_dwordx4 v139, s[80:81]
	s_mov_b32 m0, s0
	s_cmp_lg_u32 s9, -2
	s_cbranch_scc1 .Lz1_b
	v_mov_b32_e32 v60, 0
	v_mov_b32_e32 v61, 0
	v_pk_mov_b32 v[62:63], v[60:61], v[60:61]
	v_pk_mov_b32 v[56:57], v[60:61], v[60:61]
	v_pk_mov_b32 v[58:59], v[60:61], v[60:61]
	v_pk_mov_b32 v[44:45], v[60:61], v[60:61]
	v_pk_mov_b32 v[46:47], v[60:61], v[60:61]
	v_pk_mov_b32 v[40:41], v[60:61], v[60:61]
	v_pk_mov_b32 v[42:43], v[60:61], v[60:61]
	v_pk_mov_b32 v[28:29], v[60:61], v[60:61]
	v_pk_mov_b32 v[30:31], v[60:61], v[60:61]
	v_pk_mov_b32 v[24:25], v[60:61], v[60:61]
	v_pk_mov_b32 v[26:27], v[60:61], v[60:61]
	v_pk_mov_b32 v[12:13], v[60:61], v[60:61]
	v_pk_mov_b32 v[14:15], v[60:61], v[60:61]
	v_pk_mov_b32 v[0:1], v[60:61], v[60:61]
	v_pk_mov_b32 v[2:3], v[60:61], v[60:61]
	v_pk_mov_b32 v[52:53], v[60:61], v[60:61]
	v_pk_mov_b32 v[54:55], v[60:61], v[60:61]
	v_pk_mov_b32 v[48:49], v[60:61], v[60:61]
	v_pk_mov_b32 v[50:51], v[60:61], v[60:61]
	v_pk_mov_b32 v[36:37], v[60:61], v[60:61]
	v_pk_mov_b32 v[38:39], v[60:61], v[60:61]
	v_pk_mov_b32 v[32:33], v[60:61], v[60:61]
	v_pk_mov_b32 v[34:35], v[60:61], v[60:61]
	v_pk_mov_b32 v[20:21], v[60:61], v[60:61]
	v_pk_mov_b32 v[22:23], v[60:61], v[60:61]
	v_pk_mov_b32 v[16:17], v[60:61], v[60:61]
	v_pk_mov_b32 v[18:19], v[60:61], v[60:61]
	v_pk_mov_b32 v[8:9], v[60:61], v[60:61]
	v_pk_mov_b32 v[10:11], v[60:61], v[60:61]
	v_pk_mov_b32 v[4:5], v[60:61], v[60:61]
	v_pk_mov_b32 v[6:7], v[60:61], v[60:61]
.Lz1_b:
	s_waitcnt vmcnt(8)
	s_waitcnt lgkmcnt(0)
	s_barrier
	s_setprio 1
	s_waitcnt lgkmcnt(6)
	v_mfma_scale_f32_16x16x128_f8f6f4 v[60:63], v[146:153], v[64:71], v[60:63], v143, v143 op_sel_hi:[0,0,0]
	v_mfma_scale_f32_16x16x128_f8f6f4 v[56:59], v[154:161], v[64:71], v[56:59], v143, v143 op_sel_hi:[0,0,0]
	s_waitcnt lgkmcnt(4)
	v_mfma_scale_f32_16x16x128_f8f6f4 v[194:197], v[146:153], v[72:79], v[44:47], v143, v143 op_sel_hi:[0,0,0]
	v_mfma_scale_f32_16x16x128_f8f6f4 v[198:201], v[154:161], v[72:79], v[40:43], v143, v143 op_sel_hi:[0,0,0]
	s_waitcnt lgkmcnt(2)
	v_mfma_scale_f32_16x16x128_f8f6f4 v[202:205], v[146:153], v[80:87], v[28:31], v143, v143 op_sel_hi:[0,0,0]
	v_mfma_scale_f32_16x16x128_f8f6f4 v[206:209], v[154:161], v[80:87], v[24:27], v143, v143 op_sel_hi:[0,0,0]
	s_waitcnt lgkmcnt(0)
	v_mfma_scale_f32_16x16x128_f8f6f4 v[222:225], v[146:153], v[88:95], v[12:15], v143, v143 op_sel_hi:[0,0,0]
	v_mfma_scale_f32_16x16x128_f8f6f4 v[226:229], v[154:161], v[88:95], v[0:3], v143, v143 op_sel_hi:[0,0,0]
	s_setprio 0
	s_setprio 1
	v_mfma_scale_f32_16x16x128_f8f6f4 v[52:55], v[162:169], v[64:71], v[52:55], v143, v143 op_sel_hi:[0,0,0]
	v_mfma_scale_f32_16x16x128_f8f6f4 v[48:51], v[170:177], v[64:71], v[48:51], v143, v143 op_sel_hi:[0,0,0]
	v_mfma_scale_f32_16x16x128_f8f6f4 v[230:233], v[162:169], v[72:79], v[36:39], v143, v143 op_sel_hi:[0,0,0]
	v_mfma_scale_f32_16x16x128_f8f6f4 v[234:237], v[170:177], v[72:79], v[32:35], v143, v143 op_sel_hi:[0,0,0]
	v_mfma_scale_f32_16x16x128_f8f6f4 v[238:241], v[162:169], v[80:87], v[20:23], v143, v143 op_sel_hi:[0,0,0]
	v_mfma_scale_f32_16x16x128_f8f6f4 v[242:245], v[170:177], v[80:87], v[16:19], v143, v143 op_sel_hi:[0,0,0]
	v_mfma_scale_f32_16x16x128_f8f6f4 v[246:249], v[162:169], v[88:95], v[8:11], v143, v143 op_sel_hi:[0,0,0]
	v_mfma_scale_f32_16x16x128_f8f6f4 v[250:253], v[170:177], v[88:95], v[4:7], v143, v143 op_sel_hi:[0,0,0]
	s_setprio 0
	s_barrier
	ds_read_b128 v[0:3], v144
	s_nop 3
	ds_read_b128 v[4:7], v144 offset:1024
	ds_read_b128 v[16:19], v144 offset:2048
	ds_read_b128 v[20:23], v144 offset:3072
	ds_read_b128 v[146:149], v145
	ds_read_b128 v[150:153], v145 offset:1024
	ds_read_b128 v[154:157], v145 offset:2048
	ds_read_b128 v[158:161], v145 offset:3072
	ds_read_b128 v[8:11], v142 offset:32768
	ds_read_b128 v[12:15], v142 offset:33792
	ds_read_b128 v[24:27], v142 offset:34816
	ds_read_b128 v[28:31], v142 offset:35840
	ds_read_b128 v[32:35], v142 offset:36864
	ds_read_b128 v[36:39], v142 offset:37888
	ds_read_b128 v[40:43], v142 offset:38912
	ds_read_b128 v[44:47], v142 offset:39936
	s_add_u32 s34, s80, 0x40000
	s_addc_u32 s35, s81, 0
	s_mov_b32 s0, m0
	s_mov_b32 m0, s44
	s_nop 2
	global_load_lds_dwordx4 v138, s[34:35]
	s_mov_b32 m0, s0
	s_nop 0
	s_mov_b32 s0, m0
	s_mov_b32 m0, s45
	s_nop 2
	global_load_lds_dwordx4 v139, s[34:35]
	s_mov_b32 m0, s0
	s_waitcnt vmcnt(8)
	s_waitcnt lgkmcnt(0)
	s_barrier
	s_setprio 1
	s_waitcnt lgkmcnt(6)
	v_mfma_scale_f32_16x16x128_f8f6f4 v[124:127], v[0:7], v[8:15], v[124:127], v143, v143 op_sel_hi:[0,0,0]
	v_mfma_scale_f32_16x16x128_f8f6f4 v[120:123], v[16:23], v[8:15], v[120:123], v143, v143 op_sel_hi:[0,0,0]
	s_waitcnt lgkmcnt(4)
	v_mfma_scale_f32_16x16x128_f8f6f4 v[108:111], v[0:7], v[24:31], v[108:111], v143, v143 op_sel_hi:[0,0,0]
	v_mfma_scale_f32_16x16x128_f8f6f4 v[104:107], v[16:23], v[24:31], v[104:107], v143, v143 op_sel_hi:[0,0,0]
	s_waitcnt lgkmcnt(2)
	v_mfma_scale_f32_16x16x128_f8f6f4 v[92:95], v[0:7], v[32:39], v[130:133], v143, v143 op_sel_hi:[0,0,0]
	v_mfma_scale_f32_16x16x128_f8f6f4 v[88:91], v[16:23], v[32:39], v[210:213], v143, v143 op_sel_hi:[0,0,0]
	s_waitcnt lgkmcnt(0)
	v_mfma_scale_f32_16x16x128_f8f6f4 v[76:79], v[0:7], v[40:47], v[214:217], v143, v143 op_sel_hi:[0,0,0]
	v_mfma_scale_f32_16x16x128_f8f6f4 v[72:75], v[16:23], v[40:47], v[218:221], v143, v143 op_sel_hi:[0,0,0]
	s_setprio 0
	s_setprio 1
	v_mfma_scale_f32_16x16x128_f8f6f4 v[116:119], v[146:153], v[8:15], v[116:119], v143, v143 op_sel_hi:[0,0,0]
	v_mfma_scale_f32_16x16x128_f8f6f4 v[112:115], v[154:161], v[8:15], v[112:115], v143, v143 op_sel_hi:[0,0,0]
	v_mfma_scale_f32_16x16x128_f8f6f4 v[100:103], v[146:153], v[24:31], v[100:103], v143, v143 op_sel_hi:[0,0,0]
	v_mfma_scale_f32_16x16x128_f8f6f4 v[96:99], v[154:161], v[24:31], v[96:99], v143, v143 op_sel_hi:[0,0,0]
	v_mfma_scale_f32_16x16x128_f8f6f4 v[84:87], v[146:153], v[32:39], v[178:181], v143, v143 op_sel_hi:[0,0,0]
	v_mfma_scale_f32_16x16x128_f8f6f4 v[80:83], v[154:161], v[32:39], v[182:185], v143, v143 op_sel_hi:[0,0,0]
	v_mfma_scale_f32_16x16x128_f8f6f4 v[68:71], v[146:153], v[40:47], v[186:189], v143, v143 op_sel_hi:[0,0,0]
	v_mfma_scale_f32_16x16x128_f8f6f4 v[64:67], v[154:161], v[40:47], v[190:193], v143, v143 op_sel_hi:[0,0,0]
	s_setprio 0
	s_barrier
	ds_read_b128 v[32:35], v142 offset:49152
	ds_read_b128 v[36:39], v142 offset:50176
	ds_read_b128 v[162:165], v142 offset:51200
	ds_read_b128 v[166:169], v142 offset:52224
	ds_read_b128 v[170:173], v142 offset:53248
	ds_read_b128 v[174:177], v142 offset:54272
	ds_read_b128 v[178:181], v142 offset:55296
	ds_read_b128 v[182:185], v142 offset:56320
	s_mov_b32 s0, m0
	s_mov_b32 m0, s46
	s_nop 2
	global_load_lds_dwordx4 v136, s[78:79]
	s_mov_b32 m0, s0
	s_add_u32 s34, s62, 0x80
	s_mov_b32 s0, m0
	s_mov_b32 m0, s48
	s_nop 2
	global_load_lds_dwordx4 v137, s[78:79]
	s_mov_b32 m0, s0
	s_addc_u32 s35, s63, 0
	s_mov_b32 s0, m0
	s_mov_b32 m0, s51
	s_nop 2
	global_load_lds_dwordx4 v136, s[34:35]
	s_mov_b32 m0, s0
	s_nop 0
	s_mov_b32 s0, m0
	s_mov_b32 m0, s52
	s_nop 2
	global_load_lds_dwordx4 v137, s[34:35]
	s_mov_b32 m0, s0
	s_nop 0
	s_mov_b32 s0, m0
	s_mov_b32 m0, s49
	s_nop 2
	global_load_lds_dwordx4 v138, s[76:77]
	s_mov_b32 m0, s0
	s_nop 0
	s_mov_b32 s0, m0
	s_mov_b32 m0, s50
	s_nop 2
	global_load_lds_dwordx4 v139, s[76:77]
	s_mov_b32 m0, s0
	s_waitcnt vmcnt(8)
	s_waitcnt lgkmcnt(0)
	s_barrier
	s_setprio 1
	s_waitcnt lgkmcnt(6)
	v_mfma_scale_f32_16x16x128_f8f6f4 v[60:63], v[0:7], v[32:39], v[60:63], v143, v143 op_sel_hi:[0,0,0]
	v_mfma_scale_f32_16x16x128_f8f6f4 v[56:59], v[16:23], v[32:39], v[56:59], v143, v143 op_sel_hi:[0,0,0]
	s_waitcnt lgkmcnt(4)
	v_mfma_scale_f32_16x16x128_f8f6f4 v[44:47], v[0:7], v[162:169], v[194:197], v143, v143 op_sel_hi:[0,0,0]
	v_mfma_scale_f32_16x16x128_f8f6f4 v[40:43], v[16:23], v[162:169], v[198:201], v143, v143 op_sel_hi:[0,0,0]
	s_waitcnt lgkmcnt(2)
	v_mfma_scale_f32_16x16x128_f8f6f4 v[28:31], v[0:7], v[170:177], v[202:205], v143, v143 op_sel_hi:[0,0,0]
	v_mfma_scale_f32_16x16x128_f8f6f4 v[24:27], v[16:23], v[170:177], v[206:209], v143, v143 op_sel_hi:[0,0,0]
	s_waitcnt lgkmcnt(0)
	v_mfma_scale_f32_16x16x128_f8f6f4 v[12:15], v[0:7], v[178:185], v[222:225], v143, v143 op_sel_hi:[0,0,0]
	v_mfma_scale_f32_16x16x128_f8f6f4 v[0:3], v[16:23], v[178:185], v[226:229], v143, v143 op_sel_hi:[0,0,0]
	s_setprio 0
	s_setprio 1
	v_mfma_scale_f32_16x16x128_f8f6f4 v[52:55], v[146:153], v[32:39], v[52:55], v143, v143 op_sel_hi:[0,0,0]
	v_mfma_scale_f32_16x16x128_f8f6f4 v[48:51], v[154:161], v[32:39], v[48:51], v143, v143 op_sel_hi:[0,0,0]
	v_mfma_scale_f32_16x16x128_f8f6f4 v[36:39], v[146:153], v[162:169], v[230:233], v143, v143 op_sel_hi:[0,0,0]
	v_mfma_scale_f32_16x16x128_f8f6f4 v[32:35], v[154:161], v[162:169], v[234:237], v143, v143 op_sel_hi:[0,0,0]
	v_mfma_scale_f32_16x16x128_f8f6f4 v[20:23], v[146:153], v[170:177], v[238:241], v143, v143 op_sel_hi:[0,0,0]
	v_mfma_scale_f32_16x16x128_f8f6f4 v[16:19], v[154:161], v[170:177], v[242:245], v143, v143 op_sel_hi:[0,0,0]
	v_mfma_scale_f32_16x16x128_f8f6f4 v[8:11], v[146:153], v[178:185], v[246:249], v143, v143 op_sel_hi:[0,0,0]
	v_mfma_scale_f32_16x16x128_f8f6f4 v[4:7], v[154:161], v[178:185], v[250:253], v143, v143 op_sel_hi:[0,0,0]
	s_setprio 0
	s_barrier
	s_add_i32 s9, s9, 2
	s_add_u32 s8, s8, 0x100
	s_addc_u32 s6, s6, 0
	s_add_u32 s7, s7, 0x100
	s_addc_u32 s33, s33, 0
	s_cmp_gt_u32 s9, 13
	s_mov_b64 s[34:35], s[36:37]
	s_cbranch_scc0 .LBB0_198
	s_and_b64 vcc, exec, s[16:17]
	s_cbranch_vccz .LBB0_201
	s_barrier

.LBB0_1035:
	v_mbcnt_lo_u32_b32 v4, -1, 0
	v_mbcnt_hi_u32_b32 v4, -1, v4
	s_add_u32 s19, s50, 0x100
	v_add_u32_e32 v4, s0, v4
	v_lshl_add_u32 v4, v4, 4, 0
	v_add_u32_e32 v4, 0x21000, v4
	s_addc_u32 s25, s51, 0
	ds_write_b128 v4, v[0:3]
	s_add_u32 s81, s56, 0x100
	s_addc_u32 s82, s57, 0
	s_mov_b32 s83, -2
	s_branch .LBB0_1037
.LBB0_1036:
	s_add_u32 s50, s36, 0x100
	s_addc_u32 s51, s37, 0
	s_and_b64 s[56:57], s[58:59], exec
	s_cselect_b32 s64, s30, s19
	s_cselect_b32 s65, s31, s25
	s_cselect_b32 s63, s29, s82
	s_cselect_b32 s62, s28, s81
	s_add_u32 s56, s64, 0x80
	v_add_u32_e32 v144, 0x10000, v254
	s_addc_u32 s57, s65, 0
	ds_read_b128 v[116:119], v144
	ds_read_b128 v[120:123], v144 offset:1024
	ds_read_b128 v[156:159], v144 offset:2048
	ds_read_b128 v[160:163], v144 offset:3072
	v_add_u32_e32 v144, 0x14000, v254
	s_add_u32 s72, s36, 0x80
	ds_read_b128 v[164:167], v144
	ds_read_b128 v[168:171], v144 offset:1024
	ds_read_b128 v[172:175], v144 offset:2048
	ds_read_b128 v[176:179], v144 offset:3072
	s_addc_u32 s73, s37, 0
	s_and_b64 s[36:37], s[58:59], exec
	s_cselect_b32 s60, s34, s50
	s_cselect_b32 s61, s35, s51
	s_add_u32 s36, s60, 0x80
	s_addc_u32 s37, s61, 0
	s_add_u32 s58, s62, 0x80
	s_addc_u32 s59, s63, 0
	ds_read_b128 v[180:183], v152
	ds_read_b128 v[184:187], v152 offset:1024
	ds_read_b128 v[188:191], v152 offset:2048
	ds_read_b128 v[192:195], v152 offset:3072
	ds_read_b128 v[196:199], v152 offset:4096
	ds_read_b128 v[200:203], v152 offset:5120
	ds_read_b128 v[204:207], v152 offset:6144
	ds_read_b128 v[208:211], v152 offset:7168
	s_mov_b32 s84, m0
	s_mov_b32 m0, s55
	s_nop 2
	global_load_lds_dwordx4 v38, s[72:73]
	s_mov_b32 m0, s84
	s_nop 0
	s_mov_b32 s84, m0
	s_mov_b32 m0, s74
	s_nop 2
	global_load_lds_dwordx4 v39, s[72:73]
	s_mov_b32 m0, s84
	s_cmp_lg_u32 s83, -2
	s_cbranch_scc1 .Lz7_a
	v_mov_b32_e32 v140, 0
	v_mov_b32_e32 v141, 0
	v_pk_mov_b32 v[142:143], v[140:141], v[140:141]
	v_pk_mov_b32 v[132:133], v[140:141], v[140:141]
	v_pk_mov_b32 v[134:135], v[140:141], v[140:141]
	v_pk_mov_b32 v[124:125], v[140:141], v[140:141]
	v_pk_mov_b32 v[126:127], v[140:141], v[140:141]
	v_pk_mov_b32 v[108:109], v[140:141], v[140:141]
	v_pk_mov_b32 v[110:111], v[140:141], v[140:141]
	v_pk_mov_b32 v[96:97], v[140:141], v[140:141]
	v_pk_mov_b32 v[98:99], v[140:141], v[140:141]
	v_pk_mov_b32 v[88:89], v[140:141], v[140:141]
	v_pk_mov_b32 v[90:91], v[140:141], v[140:141]
	v_pk_mov_b32 v[80:81], v[140:141], v[140:141]
	v_pk_mov_b32 v[82:83], v[140:141], v[140:141]
	v_pk_mov_b32 v[72:73], v[140:141], v[140:141]
	v_pk_mov_b32 v[74:75], v[140:141], v[140:141]
	v_pk_mov_b32 v[136:137], v[140:141], v[140:141]
	v_pk_mov_b32 v[138:139], v[140:141], v[140:141]
	v_pk_mov_b32 v[128:129], v[140:141], v[140:141]
	v_pk_mov_b32 v[130:131], v[140:141], v[140:141]
	v_pk_mov_b32 v[112:113], v[140:141], v[140:141]
	v_pk_mov_b32 v[114:115], v[140:141], v[140:141]
	v_pk_mov_b32 v[100:101], v[140:141], v[140:141]
	v_pk_mov_b32 v[102:103], v[140:141], v[140:141]
	v_pk_mov_b32 v[92:93], v[140:141], v[140:141]
	v_pk_mov_b32 v[94:95], v[140:141], v[140:141]
	v_pk_mov_b32 v[84:85], v[140:141], v[140:141]
	v_pk_mov_b32 v[86:87], v[140:141], v[140:141]
	v_pk_mov_b32 v[76:77], v[140:141], v[140:141]
	v_pk_mov_b32 v[78:79], v[140:141], v[140:141]
	v_pk_mov_b32 v[68:69], v[140:141], v[140:141]
	v_pk_mov_b32 v[70:71], v[140:141], v[140:141]
.Lz7_a:
	s_waitcnt vmcnt(8)
	s_waitcnt lgkmcnt(0)
	s_barrier
	s_setprio 1
	s_waitcnt lgkmcnt(6)
	v_mfma_scale_f32_16x16x128_f8f6f4 v[140:143], v[116:123], v[180:187], v[140:143], v153, v153 op_sel_hi:[0,0,0]
	v_mfma_scale_f32_16x16x128_f8f6f4 v[132:135], v[156:163], v[180:187], v[132:135], v153, v153 op_sel_hi:[0,0,0]
	s_waitcnt lgkmcnt(4)
	v_mfma_scale_f32_16x16x128_f8f6f4 v[124:127], v[116:123], v[188:195], v[124:127], v153, v153 op_sel_hi:[0,0,0]
	v_mfma_scale_f32_16x16x128_f8f6f4 v[108:111], v[156:163], v[188:195], v[108:111], v153, v153 op_sel_hi:[0,0,0]
	s_waitcnt lgkmcnt(2)
	v_mfma_scale_f32_16x16x128_f8f6f4 v[144:147], v[116:123], v[196:203], v[96:99], v153, v153 op_sel_hi:[0,0,0]
	v_mfma_scale_f32_16x16x128_f8f6f4 v[212:215], v[156:163], v[196:203], v[88:91], v153, v153 op_sel_hi:[0,0,0]
	s_waitcnt lgkmcnt(0)
	v_mfma_scale_f32_16x16x128_f8f6f4 v[216:219], v[116:123], v[204:211], v[80:83], v153, v153 op_sel_hi:[0,0,0]
	v_mfma_scale_f32_16x16x128_f8f6f4 v[220:223], v[156:163], v[204:211], v[72:75], v153, v153 op_sel_hi:[0,0,0]
	s_setprio 0
	s_setprio 1
	v_mfma_scale_f32_16x16x128_f8f6f4 v[136:139], v[164:171], v[180:187], v[136:139], v153, v153 op_sel_hi:[0,0,0]
	v_mfma_scale_f32_16x16x128_f8f6f4 v[128:131], v[172:179], v[180:187], v[128:131], v153, v153 op_sel_hi:[0,0,0]
	v_mfma_scale_f32_16x16x128_f8f6f4 v[112:115], v[164:171], v[188:195], v[112:115], v153, v153 op_sel_hi:[0,0,0]
	v_mfma_scale_f32_16x16x128_f8f6f4 v[100:103], v[172:179], v[188:195], v[100:103], v153, v153 op_sel_hi:[0,0,0]
	v_mfma_scale_f32_16x16x128_f8f6f4 v[180:183], v[164:171], v[196:203], v[92:95], v153, v153 op_sel_hi:[0,0,0]
	v_mfma_scale_f32_16x16x128_f8f6f4 v[184:187], v[172:179], v[196:203], v[84:87], v153, v153 op_sel_hi:[0,0,0]
	v_mfma_scale_f32_16x16x128_f8f6f4 v[188:191], v[164:171], v[204:211], v[76:79], v153, v153 op_sel_hi:[0,0,0]
	v_mfma_scale_f32_16x16x128_f8f6f4 v[192:195], v[172:179], v[204:211], v[68:71], v153, v153 op_sel_hi:[0,0,0]
	s_setprio 0
	s_barrier
	s_nop 4
	ds_read_b128 v[68:71], v152 offset:16384
	ds_read_b128 v[72:75], v152 offset:17408
	ds_read_b128 v[76:79], v152 offset:18432
	ds_read_b128 v[80:83], v152 offset:19456
	ds_read_b128 v[84:87], v152 offset:20480
	ds_read_b128 v[88:91], v152 offset:21504
	ds_read_b128 v[92:95], v152 offset:22528
	ds_read_b128 v[96:99], v152 offset:23552
	s_mov_b32 s72, m0
	s_mov_b32 m0, s3
	s_nop 2
	global_load_lds_dwordx4 v252, s[64:65]
	s_mov_b32 m0, s72
	s_nop 0
	s_mov_b32 s72, m0
	s_mov_b32 m0, s27
	s_nop 2
	global_load_lds_dwordx4 v253, s[64:65]
	s_mov_b32 m0, s72
	s_mov_b32 s64, m0
	s_mov_b32 m0, s33
	s_nop 2
	global_load_lds_dwordx4 v252, s[62:63]
	s_mov_b32 m0, s64
	s_nop 0
	s_mov_b32 s64, m0
	s_mov_b32 m0, s40
	s_nop 2
	global_load_lds_dwordx4 v253, s[62:63]
	s_mov_b32 m0, s64
	s_mov_b32 s62, m0
	s_mov_b32 m0, s2
	s_nop 2
	global_load_lds_dwordx4 v104, s[60:61]
	s_mov_b32 m0, s62
	s_nop 0
	s_mov_b32 s62, m0
	s_mov_b32 m0, s41
	s_nop 2
	global_load_lds_dwordx4 v105, s[60:61]
	s_mov_b32 m0, s62
	s_cmp_lg_u32 s83, -2
	s_cbranch_scc1 .Lz7_b
	v_mov_b32_e32 v64, 0
	v_mov_b32_e32 v65, 0
	v_pk_mov_b32 v[66:67], v[64:65], v[64:65]
	v_pk_mov_b32 v[56:57], v[64:65], v[64:65]
	v_pk_mov_b32 v[58:59], v[64:65], v[64:65]
	v_pk_mov_b32 v[48:49], v[64:65], v[64:65]
	v_pk_mov_b32 v[50:51], v[64:65], v[64:65]
	v_pk_mov_b32 v[40:41], v[64:65], v[64:65]
	v_pk_mov_b32 v[42:43], v[64:65], v[64:65]
	v_pk_mov_b32 v[28:29], v[64:65], v[64:65]
	v_pk_mov_b32 v[30:31], v[64:65], v[64:65]
	v_pk_mov_b32 v[20:21], v[64:65], v[64:65]
	v_pk_mov_b32 v[22:23], v[64:65], v[64:65]
	v_pk_mov_b32 v[12:13], v[64:65], v[64:65]
	v_pk_mov_b32 v[14:15], v[64:65], v[64:65]
	v_pk_mov_b32 v[4:5], v[64:65], v[64:65]
	v_pk_mov_b32 v[6:7], v[64:65], v[64:65]
	v_pk_mov_b32 v[60:61], v[64:65], v[64:65]
	v_pk_mov_b32 v[62:63], v[64:65], v[64:65]
	v_pk_mov_b32 v[52:53], v[64:65], v[64:65]
	v_pk_mov_b32 v[54:55], v[64:65], v[64:65]
	v_pk_mov_b32 v[32:33], v[64:65], v[64:65]
	v_pk_mov_b32 v[34:35], v[64:65], v[64:65]
	v_pk_mov_b32 v[44:45], v[64:65], v[64:65]
	v_pk_mov_b32 v[46:47], v[64:65], v[64:65]
	v_pk_mov_b32 v[24:25], v[64:65], v[64:65]
	v_pk_mov_b32 v[26:27], v[64:65], v[64:65]
	v_pk_mov_b32 v[16:17], v[64:65], v[64:65]
	v_pk_mov_b32 v[18:19], v[64:65], v[64:65]
	v_pk_mov_b32 v[8:9], v[64:65], v[64:65]
	v_pk_mov_b32 v[10:11], v[64:65], v[64:65]
	v_pk_mov_b32 v[0:1], v[64:65], v[64:65]
	v_pk_mov_b32 v[2:3], v[64:65], v[64:65]
.Lz7_b:
	s_waitcnt vmcnt(8)
	s_waitcnt lgkmcnt(0)
	s_barrier
	s_cmp_lg_u32 s32, 0
	s_cbranch_scc1 .Lp7_rag_1
	s_setprio 1
	s_waitcnt lgkmcnt(6)
	v_mfma_scale_f32_16x16x128_f8f6f4 v[64:67], v[116:123], v[68:75], v[64:67], v153, v153 op_sel_hi:[0,0,0]
	v_mfma_scale_f32_16x16x128_f8f6f4 v[56:59], v[156:163], v[68:75], v[56:59], v153, v153 op_sel_hi:[0,0,0]
	s_waitcnt lgkmcnt(4)
	v_mfma_scale_f32_16x16x128_f8f6f4 v[48:51], v[116:123], v[76:83], v[48:51], v153, v153 op_sel_hi:[0,0,0]
	v_mfma_scale_f32_16x16x128_f8f6f4 v[204:207], v[156:163], v[76:83], v[40:43], v153, v153 op_sel_hi:[0,0,0]
	s_waitcnt lgkmcnt(2)
	v_mfma_scale_f32_16x16x128_f8f6f4 v[208:211], v[116:123], v[84:91], v[28:31], v153, v153 op_sel_hi:[0,0,0]
	v_mfma_scale_f32_16x16x128_f8f6f4 v[224:227], v[156:163], v[84:91], v[20:23], v153, v153 op_sel_hi:[0,0,0]
	s_waitcnt lgkmcnt(0)
	v_mfma_scale_f32_16x16x128_f8f6f4 v[228:231], v[116:123], v[92:99], v[12:15], v153, v153 op_sel_hi:[0,0,0]
	v_mfma_scale_f32_16x16x128_f8f6f4 v[232:235], v[156:163], v[92:99], v[4:7], v153, v153 op_sel_hi:[0,0,0]
	s_setprio 0
	s_setprio 1
	v_mfma_scale_f32_16x16x128_f8f6f4 v[60:63], v[164:171], v[68:75], v[60:63], v153, v153 op_sel_hi:[0,0,0]
	v_mfma_scale_f32_16x16x128_f8f6f4 v[52:55], v[172:179], v[68:75], v[52:55], v153, v153 op_sel_hi:[0,0,0]
	v_mfma_scale_f32_16x16x128_f8f6f4 v[32:35], v[172:179], v[76:83], v[32:35], v153, v153 op_sel_hi:[0,0,0]
	v_mfma_scale_f32_16x16x128_f8f6f4 v[236:239], v[164:171], v[76:83], v[44:47], v153, v153 op_sel_hi:[0,0,0]
	v_mfma_scale_f32_16x16x128_f8f6f4 v[240:243], v[164:171], v[84:91], v[24:27], v153, v153 op_sel_hi:[0,0,0]
	v_mfma_scale_f32_16x16x128_f8f6f4 v[244:247], v[172:179], v[84:91], v[16:19], v153, v153 op_sel_hi:[0,0,0]
	v_mfma_scale_f32_16x16x128_f8f6f4 v[248:251], v[164:171], v[92:99], v[8:11], v153, v153 op_sel_hi:[0,0,0]
	v_mfma_scale_f32_16x16x128_f8f6f4 v[148:151], v[172:179], v[92:99], v[0:3], v153, v153 op_sel_hi:[0,0,0]
	s_setprio 0

.LBB0_1152:
	s_and_b64 s[50:51], s[26:27], exec
	s_cselect_b32 s5, s21, s35
	s_cselect_b32 s29, s20, s34
	s_cselect_b32 s72, s23, s37
	s_cselect_b32 s73, s22, s36
	s_cselect_b32 s74, s25, s47
	s_cselect_b32 s75, s24, s46
	s_add_u32 s76, s36, 0x100
	s_addc_u32 s77, s37, 0
	s_add_u32 s78, s46, 0x100
	s_addc_u32 s79, s47, 0
	s_mov_b32 s80, -2
	s_waitcnt vmcnt(4)
.LBB0_1153:
	ds_read_b128 v[128:131], v166
	ds_read_b128 v[132:135], v166 offset:1024
	ds_read_b128 v[136:139], v166 offset:2048
	ds_read_b128 v[140:143], v166 offset:3072
	s_waitcnt vmcnt(0)
	ds_read_b128 v[144:147], v167
	ds_read_b128 v[148:151], v167 offset:1024
	ds_read_b128 v[152:155], v167 offset:2048
	ds_read_b128 v[156:159], v167 offset:3072
	s_add_u32 s36, s34, 0x100
	s_addc_u32 s37, s35, 0
	s_cmp_eq_u32 s80, 12
	s_cselect_b32 s60, s73, s76
	s_cselect_b32 s61, s72, s77
	s_cselect_b32 s47, s74, s79
	s_cselect_b32 s46, s75, s78
	s_cselect_b32 s58, s29, s36
	s_cselect_b32 s59, s5, s37
	s_add_u32 s56, s60, 0x80
	s_addc_u32 s57, s61, 0
	s_add_u32 s50, s58, 0x80
	s_addc_u32 s51, s59, 0
	ds_read_b128 v[172:175], v168
	ds_read_b128 v[176:179], v168 offset:1024
	ds_read_b128 v[180:183], v168 offset:2048
	ds_read_b128 v[184:187], v168 offset:3072
	ds_read_b128 v[188:191], v168 offset:4096
	ds_read_b128 v[192:195], v168 offset:5120
	ds_read_b128 v[196:199], v168 offset:6144
	ds_read_b128 v[200:203], v168 offset:7168
	s_add_u32 s34, s34, 0x40080
	s_addc_u32 s35, s35, 0
	s_mov_b32 s81, m0
	s_mov_b32 m0, s66
	s_nop 2
	global_load_lds_dwordx4 v164, s[34:35]
	s_mov_b32 m0, s81
	s_nop 0
	s_mov_b32 s81, m0
	s_mov_b32 m0, s67
	s_nop 2
	global_load_lds_dwordx4 v165, s[34:35]
	s_mov_b32 m0, s81
	s_cmp_lg_u32 s80, -2
	s_cbranch_scc1 .Lz8_a
	v_mov_b32_e32 v124, 0
	v_mov_b32_e32 v125, 0
	v_pk_mov_b32 v[126:127], v[124:125], v[124:125]
	v_pk_mov_b32 v[120:121], v[124:125], v[124:125]
	v_pk_mov_b32 v[122:123], v[124:125], v[124:125]
	v_pk_mov_b32 v[108:109], v[124:125], v[124:125]
	v_pk_mov_b32 v[110:111], v[124:125], v[124:125]
	v_pk_mov_b32 v[104:105], v[124:125], v[124:125]
	v_pk_mov_b32 v[106:107], v[124:125], v[124:125]
	v_pk_mov_b32 v[92:93], v[124:125], v[124:125]
	v_pk_mov_b32 v[94:95], v[124:125], v[124:125]
	v_pk_mov_b32 v[88:89], v[124:125], v[124:125]
	v_pk_mov_b32 v[90:91], v[124:125], v[124:125]
	v_pk_mov_b32 v[76:77], v[124:125], v[124:125]
	v_pk_mov_b32 v[78:79], v[124:125], v[124:125]
	v_pk_mov_b32 v[72:73], v[124:125], v[124:125]
	v_pk_mov_b32 v[74:75], v[124:125], v[124:125]
	v_pk_mov_b32 v[116:117], v[124:125], v[124:125]
	v_pk_mov_b32 v[118:119], v[124:125], v[124:125]
	v_pk_mov_b32 v[112:113], v[124:125], v[124:125]
	v_pk_mov_b32 v[114:115], v[124:125], v[124:125]
	v_pk_mov_b32 v[100:101], v[124:125], v[124:125]
	v_pk_mov_b32 v[102:103], v[124:125], v[124:125]
	v_pk_mov_b32 v[96:97], v[124:125], v[124:125]
	v_pk_mov_b32 v[98:99], v[124:125], v[124:125]
	v_pk_mov_b32 v[84:85], v[124:125], v[124:125]
	v_pk_mov_b32 v[86:87], v[124:125], v[124:125]
	v_pk_mov_b32 v[80:81], v[124:125], v[124:125]
	v_pk_mov_b32 v[82:83], v[124:125], v[124:125]
	v_pk_mov_b32 v[68:69], v[124:125], v[124:125]
	v_pk_mov_b32 v[70:71], v[124:125], v[124:125]
	v_pk_mov_b32 v[64:65], v[124:125], v[124:125]
	v_pk_mov_b32 v[66:67], v[124:125], v[124:125]
.Lz8_a:
	s_waitcnt vmcnt(8)
	s_waitcnt lgkmcnt(0)
	s_barrier
	s_setprio 1
	s_waitcnt lgkmcnt(6)
	v_mfma_scale_f32_16x16x128_f8f6f4 v[124:127], v[128:135], v[172:179], v[124:127], v169, v169 op_sel_hi:[0,0,0]
	v_mfma_scale_f32_16x16x128_f8f6f4 v[120:123], v[136:143], v[172:179], v[120:123], v169, v169 op_sel_hi:[0,0,0]
	s_waitcnt lgkmcnt(4)
	v_mfma_scale_f32_16x16x128_f8f6f4 v[108:111], v[128:135], v[180:187], v[108:111], v169, v169 op_sel_hi:[0,0,0]
	v_mfma_scale_f32_16x16x128_f8f6f4 v[104:107], v[136:143], v[180:187], v[104:107], v169, v169 op_sel_hi:[0,0,0]
	s_waitcnt lgkmcnt(2)
	v_mfma_scale_f32_16x16x128_f8f6f4 v[204:207], v[128:135], v[188:195], v[92:95], v169, v169 op_sel_hi:[0,0,0]
	v_mfma_scale_f32_16x16x128_f8f6f4 v[208:211], v[136:143], v[188:195], v[88:91], v169, v169 op_sel_hi:[0,0,0]
	s_waitcnt lgkmcnt(0)
	v_mfma_scale_f32_16x16x128_f8f6f4 v[212:215], v[128:135], v[196:203], v[76:79], v169, v169 op_sel_hi:[0,0,0]
	v_mfma_scale_f32_16x16x128_f8f6f4 v[216:219], v[136:143], v[196:203], v[72:75], v169, v169 op_sel_hi:[0,0,0]
	s_setprio 0
	s_setprio 1
	v_mfma_scale_f32_16x16x128_f8f6f4 v[116:119], v[144:151], v[172:179], v[116:119], v169, v169 op_sel_hi:[0,0,0]
	v_mfma_scale_f32_16x16x128_f8f6f4 v[112:115], v[152:159], v[172:179], v[112:115], v169, v169 op_sel_hi:[0,0,0]
	v_mfma_scale_f32_16x16x128_f8f6f4 v[100:103], v[144:151], v[180:187], v[100:103], v169, v169 op_sel_hi:[0,0,0]
	v_mfma_scale_f32_16x16x128_f8f6f4 v[96:99], v[152:159], v[180:187], v[96:99], v169, v169 op_sel_hi:[0,0,0]
	v_mfma_scale_f32_16x16x128_f8f6f4 v[172:175], v[144:151], v[188:195], v[84:87], v169, v169 op_sel_hi:[0,0,0]
	v_mfma_scale_f32_16x16x128_f8f6f4 v[176:179], v[152:159], v[188:195], v[80:83], v169, v169 op_sel_hi:[0,0,0]
	v_mfma_scale_f32_16x16x128_f8f6f4 v[180:183], v[144:151], v[196:203], v[68:71], v169, v169 op_sel_hi:[0,0,0]
	v_mfma_scale_f32_16x16x128_f8f6f4 v[184:187], v[152:159], v[196:203], v[64:67], v169, v169 op_sel_hi:[0,0,0]
	s_setprio 0
	s_barrier
	s_nop 4
	ds_read_b128 v[64:67], v168 offset:16384
	ds_read_b128 v[68:71], v168 offset:17408
	ds_read_b128 v[72:75], v168 offset:18432
	ds_read_b128 v[76:79], v168 offset:19456
	ds_read_b128 v[80:83], v168 offset:20480
	ds_read_b128 v[84:87], v168 offset:21504
	ds_read_b128 v[88:91], v168 offset:22528
	ds_read_b128 v[92:95], v168 offset:23552
	s_mov_b32 s34, m0
	s_mov_b32 m0, s31
	s_nop 2
	global_load_lds_dwordx4 v162, s[60:61]
	s_mov_b32 m0, s34
	s_nop 0
	s_mov_b32 s34, m0
	s_mov_b32 m0, s44
	s_nop 2
	global_load_lds_dwordx4 v163, s[60:61]
	s_mov_b32 m0, s34
	s_nop 0
	s_mov_b32 s34, m0
	s_mov_b32 m0, s45
	s_nop 2
	global_load_lds_dwordx4 v162, s[46:47]
	s_mov_b32 m0, s34
	s_nop 0
	s_mov_b32 s34, m0
	s_mov_b32 m0, s48
	s_nop 2
	global_load_lds_dwordx4 v163, s[46:47]
	s_mov_b32 m0, s34
	s_nop 0
	s_mov_b32 s34, m0
	s_mov_b32 m0, s2
	s_nop 2
	global_load_lds_dwordx4 v164, s[58:59]
	s_mov_b32 m0, s34
	s_nop 0
	s_mov_b32 s34, m0
	s_mov_b32 m0, s49
	s_nop 2
	global_load_lds_dwordx4 v165, s[58:59]
	s_mov_b32 m0, s34
	s_cmp_lg_u32 s80, -2
	s_cbranch_scc1 .Lz8_b
	v_mov_b32_e32 v60, 0
	v_mov_b32_e32 v61, 0
	v_pk_mov_b32 v[62:63], v[60:61], v[60:61]
	v_pk_mov_b32 v[56:57], v[60:61], v[60:61]
	v_pk_mov_b32 v[58:59], v[60:61], v[60:61]
	v_pk_mov_b32 v[44:45], v[60:61], v[60:61]
	v_pk_mov_b32 v[46:47], v[60:61], v[60:61]
	v_pk_mov_b32 v[40:41], v[60:61], v[60:61]
	v_pk_mov_b32 v[42:43], v[60:61], v[60:61]
	v_pk_mov_b32 v[24:25], v[60:61], v[60:61]
	v_pk_mov_b32 v[26:27], v[60:61], v[60:61]
	v_pk_mov_b32 v[12:13], v[60:61], v[60:61]
	v_pk_mov_b32 v[14:15], v[60:61], v[60:61]
	v_pk_mov_b32 v[4:5], v[60:61], v[60:61]
	v_pk_mov_b32 v[6:7], v[60:61], v[60:61]
	v_pk_mov_b32 v[0:1], v[60:61], v[60:61]
	v_pk_mov_b32 v[2:3], v[60:61], v[60:61]
	v_pk_mov_b32 v[52:53], v[60:61], v[60:61]
	v_pk_mov_b32 v[54:55], v[60:61], v[60:61]
	v_pk_mov_b32 v[48:49], v[60:61], v[60:61]
	v_pk_mov_b32 v[50:51], v[60:61], v[60:61]
	v_pk_mov_b32 v[28:29], v[60:61], v[60:61]
	v_pk_mov_b32 v[30:31], v[60:61], v[60:61]
	v_pk_mov_b32 v[20:21], v[60:61], v[60:61]
	v_pk_mov_b32 v[22:23], v[60:61], v[60:61]
	v_pk_mov_b32 v[36:37], v[60:61], v[60:61]
	v_pk_mov_b32 v[38:39], v[60:61], v[60:61]
	v_pk_mov_b32 v[32:33], v[60:61], v[60:61]
	v_pk_mov_b32 v[34:35], v[60:61], v[60:61]
	v_pk_mov_b32 v[16:17], v[60:61], v[60:61]
	v_pk_mov_b32 v[18:19], v[60:61], v[60:61]
	v_pk_mov_b32 v[8:9], v[60:61], v[60:61]
	v_pk_mov_b32 v[10:11], v[60:61], v[60:61]
.Lz8_b:
	s_waitcnt vmcnt(8)
	s_waitcnt lgkmcnt(0)
	s_barrier
	s_cmp_le_i32 s42, s32
	s_cbranch_scc1 .Lp8_rag_1
	s_setprio 1
	s_waitcnt lgkmcnt(6)
	v_mfma_scale_f32_16x16x128_f8f6f4 v[60:63], v[128:135], v[64:71], v[60:63], v169, v169 op_sel_hi:[0,0,0]
	v_mfma_scale_f32_16x16x128_f8f6f4 v[56:59], v[136:143], v[64:71], v[56:59], v169, v169 op_sel_hi:[0,0,0]
	s_waitcnt lgkmcnt(4)
	v_mfma_scale_f32_16x16x128_f8f6f4 v[188:191], v[128:135], v[72:79], v[44:47], v169, v169 op_sel_hi:[0,0,0]
	v_mfma_scale_f32_16x16x128_f8f6f4 v[192:195], v[136:143], v[72:79], v[40:43], v169, v169 op_sel_hi:[0,0,0]
	s_waitcnt lgkmcnt(2)
	v_mfma_scale_f32_16x16x128_f8f6f4 v[196:199], v[128:135], v[80:87], v[24:27], v169, v169 op_sel_hi:[0,0,0]
	v_mfma_scale_f32_16x16x128_f8f6f4 v[200:203], v[136:143], v[80:87], v[12:15], v169, v169 op_sel_hi:[0,0,0]
	s_waitcnt lgkmcnt(0)
	v_mfma_scale_f32_16x16x128_f8f6f4 v[220:223], v[128:135], v[88:95], v[4:7], v169, v169 op_sel_hi:[0,0,0]
	v_mfma_scale_f32_16x16x128_f8f6f4 v[224:227], v[136:143], v[88:95], v[0:3], v169, v169 op_sel_hi:[0,0,0]
	s_setprio 0
	s_setprio 1
	v_mfma_scale_f32_16x16x128_f8f6f4 v[52:55], v[144:151], v[64:71], v[52:55], v169, v169 op_sel_hi:[0,0,0]
	v_mfma_scale_f32_16x16x128_f8f6f4 v[48:51], v[152:159], v[64:71], v[48:51], v169, v169 op_sel_hi:[0,0,0]
	v_mfma_scale_f32_16x16x128_f8f6f4 v[228:231], v[144:151], v[72:79], v[28:31], v169, v169 op_sel_hi:[0,0,0]
	v_mfma_scale_f32_16x16x128_f8f6f4 v[232:235], v[152:159], v[72:79], v[20:23], v169, v169 op_sel_hi:[0,0,0]
	v_mfma_scale_f32_16x16x128_f8f6f4 v[236:239], v[144:151], v[80:87], v[36:39], v169, v169 op_sel_hi:[0,0,0]
	v_mfma_scale_f32_16x16x128_f8f6f4 v[240:243], v[152:159], v[80:87], v[32:35], v169, v169 op_sel_hi:[0,0,0]
	v_mfma_scale_f32_16x16x128_f8f6f4 v[244:247], v[144:151], v[88:95], v[16:19], v169, v169 op_sel_hi:[0,0,0]
	v_mfma_scale_f32_16x16x128_f8f6f4 v[248:251], v[152:159], v[88:95], v[8:11], v169, v169 op_sel_hi:[0,0,0]
	s_setprio 0
